# v57 + MLA: per-lane half-row partial sums in the loop, one lane exchange of the row sum per unit
# speedup vs baseline: 1.0043x; 1.0043x over previous
.LBB0_851:
	v_exp_f32_e32 v101, v80
	v_exp_f32_e32 v103, v81
	v_exp_f32_e32 v111, v88
	v_exp_f32_e32 v89, v89
	v_exp_f32_e32 v105, v82
	v_exp_f32_e32 v113, v90
	v_exp_f32_e32 v83, v83
	v_exp_f32_e32 v91, v91
	v_exp_f32_e32 v107, v84
	v_exp_f32_e32 v115, v92
	v_mov_b32_e32 v100, v64
	v_mov_b32_e32 v102, v65
	v_mov_b32_e32 v110, v72
	v_mov_b32_e32 v88, v73
	v_exp_f32_e32 v85, v85
	v_exp_f32_e32 v93, v93
	v_pk_add_f32 v[80:81], v[100:101], v[102:103]
	v_pk_add_f32 v[118:119], v[110:111], v[88:89]
	v_mov_b32_e32 v104, v66
	v_mov_b32_e32 v112, v74
	v_exp_f32_e32 v109, v86
	v_exp_f32_e32 v117, v94
	v_pk_add_f32 v[80:81], v[104:105], v[80:81]
	v_pk_add_f32 v[118:119], v[112:113], v[118:119]
	v_mov_b32_e32 v82, v67
	v_mov_b32_e32 v90, v75
	v_exp_f32_e32 v87, v87
	v_exp_f32_e32 v95, v95
	v_pk_add_f32 v[80:81], v[82:83], v[80:81]
	v_pk_add_f32 v[118:119], v[90:91], v[118:119]
	v_mov_b32_e32 v106, v68
	v_mov_b32_e32 v114, v76
	v_pk_add_f32 v[80:81], v[106:107], v[80:81]
	v_pk_add_f32 v[118:119], v[114:115], v[118:119]
	v_mov_b32_e32 v84, v69
	v_mov_b32_e32 v92, v77
	v_pk_add_f32 v[80:81], v[84:85], v[80:81]
	v_pk_add_f32 v[118:119], v[92:93], v[118:119]
	v_mov_b32_e32 v108, v70
	v_mov_b32_e32 v116, v78
	v_pk_add_f32 v[80:81], v[108:109], v[80:81]
	v_pk_add_f32 v[118:119], v[116:117], v[118:119]
	v_mov_b32_e32 v86, v71
	v_mov_b32_e32 v94, v79
	v_pk_add_f32 v[80:81], v[86:87], v[80:81]
	v_pk_add_f32 v[118:119], v[94:95], v[118:119]
	s_lshl_b32 s2, s63, 12
	v_pk_add_f32 v[80:81], v[118:119], v[80:81]
	s_add_u32 s16, s35, s2
	v_pk_add_f32 v[80:81], v[80:81], v[80:81] op_sel:[0,1] op_sel_hi:[1,0]
	s_addc_u32 s17, s36, 0
	s_lshl_b32 s2, s33, 7
	v_fmac_f32_e32 v80, v210, v200
	v_mov_b32_e32 v99, v80
	s_ashr_i32 s3, s2, 31
	s_nop 0
	v_permlane32_swap_b32_e32 v80, v99
	s_lshl_b64 s[2:3], s[2:3], 1
	v_mov_b32_e32 v96, 0
	v_add_f32_e32 v98, v142, v143
	v_mov_b32_e32 v97, v80
	s_add_u32 s16, s16, s2
	v_pk_add_f32 v[80:81], v[96:97], v[98:99]
	v_cvt_pk_bf16_f32 v64, v64, v65
	v_cvt_pk_bf16_f32 v65, v66, v67
	v_cvt_pk_bf16_f32 v66, v68, v69
	v_cvt_pk_bf16_f32 v67, v70, v71
	v_cvt_pk_bf16_f32 v68, v72, v73
	v_cvt_pk_bf16_f32 v69, v74, v75
	v_cvt_pk_bf16_f32 v70, v76, v77
	v_cvt_pk_bf16_f32 v71, v78, v79
	v_cvt_pk_bf16_f32 v72, v101, v103
	v_cvt_pk_bf16_f32 v73, v105, v83
	v_cvt_pk_bf16_f32 v74, v107, v85
	v_cvt_pk_bf16_f32 v75, v109, v87
	v_cvt_pk_bf16_f32 v76, v111, v89
	v_cvt_pk_bf16_f32 v77, v113, v91
	v_cvt_pk_bf16_f32 v78, v115, v93
	v_cvt_pk_bf16_f32 v79, v117, v95
	s_addc_u32 s17, s17, s3
	v_fmac_f32_e32 v81, v80, v128
	ds_read_b64_tr_b16 v[82:83], v203 offset:0
	ds_read_b64_tr_b16 v[84:85], v203 offset:0x800
	ds_read_b64_tr_b16 v[86:87], v203 offset:0x1000
	ds_read_b64_tr_b16 v[88:89], v203 offset:0x1800
	ds_read_b64_tr_b16 v[90:91], v203 offset:0x2000
	ds_read_b64_tr_b16 v[92:93], v203 offset:0x2800
	ds_read_b64_tr_b16 v[94:95], v203 offset:0x3000
	ds_read_b64_tr_b16 v[96:97], v203 offset:0x3800
	s_waitcnt lgkmcnt(0)
	s_nop 0
	v_mfma_f32_32x32x16_bf16 v[0:15], v[82:85], v[64:67], v[0:15]
	ds_read_b64_tr_b16 v[82:83], v203 offset:0x200
	ds_read_b64_tr_b16 v[84:85], v203 offset:0xa00
	v_mfma_f32_32x32x16_bf16 v[0:15], v[86:89], v[68:71], v[0:15]
	ds_read_b64_tr_b16 v[86:87], v203 offset:0x1200
	ds_read_b64_tr_b16 v[88:89], v203 offset:0x1a00
	v_mfma_f32_32x32x16_bf16 v[0:15], v[90:93], v[72:75], v[0:15]
	ds_read_b64_tr_b16 v[90:91], v203 offset:0x2200
	ds_read_b64_tr_b16 v[92:93], v203 offset:0x2a00
	v_mfma_f32_32x32x16_bf16 v[0:15], v[94:97], v[76:79], v[0:15]
	ds_read_b64_tr_b16 v[94:95], v203 offset:0x3200
	ds_read_b64_tr_b16 v[96:97], v203 offset:0x3a00
	s_waitcnt lgkmcnt(0)
	v_mfma_f32_32x32x16_bf16 v[48:63], v[82:85], v[64:67], v[48:63]
	ds_read_b64_tr_b16 v[82:83], v203 offset:0x400
	ds_read_b64_tr_b16 v[84:85], v203 offset:0xc00
	v_mfma_f32_32x32x16_bf16 v[48:63], v[86:89], v[68:71], v[48:63]
	ds_read_b64_tr_b16 v[86:87], v203 offset:0x1400
	ds_read_b64_tr_b16 v[88:89], v203 offset:0x1c00
	v_mfma_f32_32x32x16_bf16 v[48:63], v[90:93], v[72:75], v[48:63]
	ds_read_b64_tr_b16 v[90:91], v203 offset:0x2400
	ds_read_b64_tr_b16 v[92:93], v203 offset:0x2c00
	v_mfma_f32_32x32x16_bf16 v[48:63], v[94:97], v[76:79], v[48:63]
	ds_read_b64_tr_b16 v[94:95], v203 offset:0x3400
	ds_read_b64_tr_b16 v[96:97], v203 offset:0x3c00
	s_waitcnt lgkmcnt(0)
	v_mfma_f32_32x32x16_bf16 v[32:47], v[82:85], v[64:67], v[32:47]
	ds_read_b64_tr_b16 v[82:83], v203 offset:0x600
	ds_read_b64_tr_b16 v[84:85], v203 offset:0xe00
	v_mfma_f32_32x32x16_bf16 v[32:47], v[86:89], v[68:71], v[32:47]
	ds_read_b64_tr_b16 v[86:87], v203 offset:0x1600
	ds_read_b64_tr_b16 v[88:89], v203 offset:0x1e00
	v_mfma_f32_32x32x16_bf16 v[32:47], v[90:93], v[72:75], v[32:47]
	ds_read_b64_tr_b16 v[90:91], v203 offset:0x2600
	ds_read_b64_tr_b16 v[92:93], v203 offset:0x2e00
	v_mfma_f32_32x32x16_bf16 v[32:47], v[94:97], v[76:79], v[32:47]
	ds_read_b64_tr_b16 v[94:95], v203 offset:0x3600
	ds_read_b64_tr_b16 v[96:97], v203 offset:0x3e00
	s_waitcnt lgkmcnt(0)
	v_mfma_f32_32x32x16_bf16 v[16:31], v[82:85], v[64:67], v[16:31]
	v_rcp_f32_e32 v67, v81
	v_mbcnt_lo_u32_b32 v66, -1, 0
	v_mbcnt_hi_u32_b32 v66, -1, v66
	s_add_i32 s91, s91, 1
	v_add_u32_e32 v64, s80, v66
	v_ashrrev_i32_e32 v64, 1, v64
	v_mul_f32_e32 v0, v67, v0
	v_mul_f32_e32 v1, v67, v1
	v_bfi_b32 v64, s84, v64, v66
	v_cvt_pk_bf16_f32 v0, v0, v1
	v_mul_f32_e32 v1, v67, v2
	v_mul_f32_e32 v2, v67, v3
	v_ashrrev_i32_e32 v65, 31, v64
	v_cvt_pk_bf16_f32 v1, v1, v2
	v_mul_f32_e32 v2, v67, v4
	v_mul_f32_e32 v3, v67, v5
	v_lshlrev_b64 v[64:65], 12, v[64:65]
	v_lshrrev_b32_e32 v66, 1, v66
	v_cvt_pk_bf16_f32 v2, v2, v3
	v_mul_f32_e32 v3, v67, v6
	v_lshl_add_u64 v[64:65], s[16:17], 0, v[64:65]
	v_and_b32_e32 v128, 16, v66
	v_mul_f32_e32 v4, v67, v7
	v_cvt_pk_bf16_f32 v3, v3, v4
	v_lshl_add_u64 v[64:65], v[64:65], 0, v[128:129]
	v_permlane32_swap_b32_e32 v0, v2
	v_permlane32_swap_b32_e32 v1, v3
	global_store_dwordx4 v[64:65], v[0:3], off
	v_mul_f32_e32 v4, v67, v15
	v_mfma_f32_32x32x16_bf16 v[16:31], v[86:89], v[68:71], v[16:31]
	v_mul_f32_e32 v0, v67, v8
	v_mul_f32_e32 v1, v67, v9
	v_cvt_pk_bf16_f32 v0, v0, v1
	v_mul_f32_e32 v1, v67, v10
	v_mul_f32_e32 v2, v67, v11
	v_cvt_pk_bf16_f32 v1, v1, v2
	v_mul_f32_e32 v2, v67, v12
	v_mul_f32_e32 v3, v67, v13
	v_cvt_pk_bf16_f32 v2, v2, v3
	v_mul_f32_e32 v3, v67, v14
	v_cvt_pk_bf16_f32 v3, v3, v4
	v_permlane32_swap_b32_e32 v0, v2
	s_nop 0
	v_permlane32_swap_b32_e32 v1, v3
	global_store_dwordx4 v[64:65], v[0:3], off offset:32
	v_mul_f32_e32 v4, v67, v55
	v_mfma_f32_32x32x16_bf16 v[16:31], v[90:93], v[72:75], v[16:31]
	v_mul_f32_e32 v0, v67, v48
	v_mul_f32_e32 v1, v67, v49
	v_cvt_pk_bf16_f32 v0, v0, v1
	v_mul_f32_e32 v1, v67, v50
	v_mul_f32_e32 v2, v67, v51
	v_cvt_pk_bf16_f32 v1, v1, v2
	v_mul_f32_e32 v2, v67, v52
	v_mul_f32_e32 v3, v67, v53
	v_cvt_pk_bf16_f32 v2, v2, v3
	v_mul_f32_e32 v3, v67, v54
	v_cvt_pk_bf16_f32 v3, v3, v4
	v_permlane32_swap_b32_e32 v0, v2
	s_nop 0
	v_permlane32_swap_b32_e32 v1, v3
	global_store_dwordx4 v[64:65], v[0:3], off offset:64
	v_mul_f32_e32 v4, v67, v63
	v_mfma_f32_32x32x16_bf16 v[16:31], v[94:97], v[76:79], v[16:31]
	v_mul_f32_e32 v0, v67, v56
	v_mul_f32_e32 v1, v67, v57
	v_cvt_pk_bf16_f32 v0, v0, v1
	v_mul_f32_e32 v1, v67, v58
	v_mul_f32_e32 v2, v67, v59
	v_cvt_pk_bf16_f32 v1, v1, v2
	v_mul_f32_e32 v2, v67, v60
	v_mul_f32_e32 v3, v67, v61
	v_cvt_pk_bf16_f32 v2, v2, v3
	v_mul_f32_e32 v3, v67, v62
	v_cvt_pk_bf16_f32 v3, v3, v4
	v_permlane32_swap_b32_e32 v0, v2
	s_nop 0
	v_permlane32_swap_b32_e32 v1, v3
	global_store_dwordx4 v[64:65], v[0:3], off offset:96
	v_mul_f32_e32 v4, v67, v39
	s_lshl_b32 s2, s91, 8
	v_mul_f32_e32 v0, v67, v32
	v_mul_f32_e32 v1, v67, v33
	v_cvt_pk_bf16_f32 v0, v0, v1
	v_mul_f32_e32 v1, v67, v34
	v_mul_f32_e32 v2, v67, v35
	v_cvt_pk_bf16_f32 v1, v1, v2
	v_mul_f32_e32 v2, v67, v36
	v_mul_f32_e32 v3, v67, v37
	v_cvt_pk_bf16_f32 v2, v2, v3
	v_mul_f32_e32 v3, v67, v38
	v_cvt_pk_bf16_f32 v3, v3, v4
	v_permlane32_swap_b32_e32 v0, v2
	s_nop 0
	v_permlane32_swap_b32_e32 v1, v3
	global_store_dwordx4 v[64:65], v[0:3], off offset:128
	v_mul_f32_e32 v4, v67, v47
	s_add_i32 s3, s2, s94
	v_mul_f32_e32 v0, v67, v40
	v_mul_f32_e32 v1, v67, v41
	v_cvt_pk_bf16_f32 v0, v0, v1
	v_mul_f32_e32 v1, v67, v42
	v_mul_f32_e32 v2, v67, v43
	v_cvt_pk_bf16_f32 v1, v1, v2
	v_mul_f32_e32 v2, v67, v44
	v_mul_f32_e32 v3, v67, v45
	v_cvt_pk_bf16_f32 v2, v2, v3
	v_mul_f32_e32 v3, v67, v46
	v_cvt_pk_bf16_f32 v3, v3, v4
	v_permlane32_swap_b32_e32 v0, v2
	s_nop 0
	v_permlane32_swap_b32_e32 v1, v3
	global_store_dwordx4 v[64:65], v[0:3], off offset:160
	v_mul_f32_e32 v4, v67, v23
	s_cmp_lt_i32 s3, s37
	v_mul_f32_e32 v0, v67, v16
	v_mul_f32_e32 v1, v67, v17
	v_cvt_pk_bf16_f32 v0, v0, v1
	v_mul_f32_e32 v1, v67, v18
	v_mul_f32_e32 v2, v67, v19
	v_cvt_pk_bf16_f32 v1, v1, v2
	v_mul_f32_e32 v2, v67, v20
	v_mul_f32_e32 v3, v67, v21
	v_cvt_pk_bf16_f32 v2, v2, v3
	v_mul_f32_e32 v3, v67, v22
	v_cvt_pk_bf16_f32 v3, v3, v4
	v_permlane32_swap_b32_e32 v0, v2
	s_nop 0
	v_permlane32_swap_b32_e32 v1, v3
	global_store_dwordx4 v[64:65], v[0:3], off offset:192
	v_mul_f32_e32 v4, v67, v31
	s_nop 0
	v_mul_f32_e32 v0, v67, v24
	v_mul_f32_e32 v1, v67, v25
	v_cvt_pk_bf16_f32 v0, v0, v1
	v_mul_f32_e32 v1, v67, v26
	v_mul_f32_e32 v2, v67, v27
	v_cvt_pk_bf16_f32 v1, v1, v2
	v_mul_f32_e32 v2, v67, v28
	v_mul_f32_e32 v3, v67, v29
	v_cvt_pk_bf16_f32 v2, v2, v3
	v_mul_f32_e32 v3, v67, v30
	v_cvt_pk_bf16_f32 v3, v3, v4
	v_permlane32_swap_b32_e32 v0, v2
	s_nop 0
	v_permlane32_swap_b32_e32 v1, v3
	global_store_dwordx4 v[64:65], v[0:3], off offset:224
	s_cbranch_scc0 .LBB0_904

.LBB0_861:
	ds_read_b128 v[96:99], v209 offset:49152
	ds_read_b128 v[100:103], v209 offset:57344
	ds_read_b128 v[162:165], v211 offset:49152
	ds_read_b128 v[166:169], v211 offset:57344
	s_add_i32 s2, 0, 0x12000
	v_add_u32_e32 v233, s2, v218
	s_waitcnt lgkmcnt(3)
	v_mfma_f32_32x32x16_bf16 v[112:127], v[96:99], v[158:161], 0
	v_add_u32_e32 v234, s2, v220
	v_add_u32_e32 v236, s2, v222
	v_add_u32_e32 v235, s2, v224
	v_exp_f32_e32 v80, v80
	v_exp_f32_e32 v81, v81
	v_exp_f32_e32 v82, v82
	v_exp_f32_e32 v83, v83
	s_waitcnt lgkmcnt(2)
	v_mfma_f32_32x32x16_bf16 v[96:111], v[100:103], v[158:161], 0
	v_exp_f32_e32 v84, v84
	v_exp_f32_e32 v92, v92
	v_exp_f32_e32 v85, v85
	v_exp_f32_e32 v93, v93
	v_exp_f32_e32 v86, v86
	v_exp_f32_e32 v94, v94
	v_exp_f32_e32 v87, v87
	s_waitcnt lgkmcnt(1)
	v_mfma_f32_32x32x16_bf16 v[112:127], v[162:165], v[154:157], v[112:127]
	v_exp_f32_e32 v95, v95
	s_waitcnt lgkmcnt(0)
	v_mfma_f32_32x32x16_bf16 v[96:111], v[166:169], v[154:157], v[96:111]
	ds_read_b128 v[162:165], v212 offset:49152
	ds_read_b128 v[166:169], v212 offset:57344
	s_waitcnt lgkmcnt(1)
	v_mfma_f32_32x32x16_bf16 v[112:127], v[162:165], v[150:153], v[112:127]
	s_waitcnt lgkmcnt(0)
	v_mfma_f32_32x32x16_bf16 v[96:111], v[166:169], v[150:153], v[96:111]
	ds_read_b128 v[162:165], v213 offset:49152
	ds_read_b128 v[166:169], v213 offset:57344
	s_waitcnt lgkmcnt(1)
	v_mfma_f32_32x32x16_bf16 v[112:127], v[162:165], v[146:149], v[112:127]
	s_waitcnt lgkmcnt(0)
	v_mfma_f32_32x32x16_bf16 v[96:111], v[166:169], v[146:149], v[96:111]
	ds_read_b128 v[162:165], v215 offset:49152
	ds_read_b128 v[166:169], v215 offset:57344
	s_waitcnt lgkmcnt(1)
	v_mfma_f32_32x32x16_bf16 v[112:127], v[162:165], v[142:145], v[112:127]
	s_waitcnt lgkmcnt(0)
	v_mfma_f32_32x32x16_bf16 v[96:111], v[166:169], v[142:145], v[96:111]
	ds_read_b128 v[162:165], v217 offset:49152
	ds_read_b128 v[166:169], v217 offset:57344
	s_waitcnt lgkmcnt(1)
	v_mfma_f32_32x32x16_bf16 v[112:127], v[162:165], v[138:141], v[112:127]
	s_waitcnt lgkmcnt(0)
	v_mfma_f32_32x32x16_bf16 v[96:111], v[166:169], v[138:141], v[96:111]
	ds_read_b128 v[162:165], v214 offset:49152
	ds_read_b128 v[166:169], v214 offset:57344
	s_waitcnt lgkmcnt(1)
	v_mfma_f32_32x32x16_bf16 v[112:127], v[162:165], v[134:137], v[112:127]
	s_waitcnt lgkmcnt(0)
	v_mfma_f32_32x32x16_bf16 v[96:111], v[166:169], v[134:137], v[96:111]
	ds_read_b128 v[162:165], v216 offset:49152
	ds_read_b128 v[166:169], v216 offset:57344
	s_waitcnt lgkmcnt(1)
	v_mfma_f32_32x32x16_bf16 v[112:127], v[162:165], v[130:133], v[112:127]
	s_waitcnt lgkmcnt(0)
	v_mfma_f32_32x32x16_bf16 v[96:111], v[166:169], v[130:133], v[96:111]
	ds_read_b128 v[162:165], v233
	ds_read_b128 v[166:169], v233 offset:4096
	ds_read_b128 v[170:173], v204
	s_waitcnt lgkmcnt(0)
	v_mfma_f32_32x32x16_bf16 v[112:127], v[162:165], v[170:173], v[112:127]
	v_mfma_f32_32x32x16_bf16 v[96:111], v[166:169], v[170:173], v[96:111]
	ds_read_b128 v[162:165], v234
	ds_read_b128 v[166:169], v234 offset:4096
	ds_read_b128 v[170:173], v204 offset:1024
	s_waitcnt lgkmcnt(0)
	v_mfma_f32_32x32x16_bf16 v[112:127], v[162:165], v[170:173], v[112:127]
	v_mfma_f32_32x32x16_bf16 v[96:111], v[166:169], v[170:173], v[96:111]
	ds_read_b128 v[162:165], v236
	ds_read_b128 v[166:169], v236 offset:4096
	ds_read_b128 v[170:173], v204 offset:2048
	s_waitcnt lgkmcnt(0)
	v_mfma_f32_32x32x16_bf16 v[112:127], v[162:165], v[170:173], v[112:127]
	v_mfma_f32_32x32x16_bf16 v[96:111], v[166:169], v[170:173], v[96:111]
	ds_read_b128 v[162:165], v235
	ds_read_b128 v[166:169], v235 offset:4096
	ds_read_b128 v[170:173], v204 offset:3072
	s_waitcnt lgkmcnt(0)
	v_mfma_f32_32x32x16_bf16 v[112:127], v[162:165], v[170:173], v[112:127]
	v_exp_f32_e32 v162, v88
	v_exp_f32_e32 v163, v89
	v_exp_f32_e32 v164, v90
	v_exp_f32_e32 v165, v91
	v_add_f32_e32 v88, v64, v65
	v_add_f32_e32 v89, v72, v73
	v_add_f32_e32 v90, v80, v81
	v_add_f32_e32 v91, v162, v163
	v_add_f32_e32 v88, v66, v88
	v_add_f32_e32 v89, v74, v89
	v_add_f32_e32 v90, v82, v90
	v_add_f32_e32 v91, v164, v91
	v_add_f32_e32 v88, v67, v88
	v_add_f32_e32 v89, v75, v89
	v_add_f32_e32 v90, v83, v90
	v_add_f32_e32 v91, v165, v91
	v_add_f32_e32 v88, v68, v88
	v_add_f32_e32 v89, v76, v89
	v_add_f32_e32 v90, v84, v90
	v_add_f32_e32 v91, v92, v91
	v_add_f32_e32 v88, v69, v88
	v_add_f32_e32 v89, v77, v89
	v_add_f32_e32 v90, v85, v90
	v_add_f32_e32 v91, v93, v91
	v_add_f32_e32 v88, v70, v88
	v_add_f32_e32 v89, v78, v89
	v_add_f32_e32 v90, v86, v90
	v_add_f32_e32 v91, v94, v91
	v_add_f32_e32 v88, v71, v88
	v_add_f32_e32 v89, v79, v89
	v_add_f32_e32 v90, v87, v90
	v_add_f32_e32 v91, v95, v91
	v_add_f32_e32 v88, v89, v88
	v_add_f32_e32 v89, v91, v90
	v_add_f32_e32 v237, v88, v89
	v_cvt_pk_bf16_f32 v88, v64, v65
	v_cvt_pk_bf16_f32 v89, v66, v67
	v_cvt_pk_bf16_f32 v90, v68, v69
	v_cvt_pk_bf16_f32 v91, v70, v71
	v_cvt_pk_bf16_f32 v72, v72, v73
	v_cvt_pk_bf16_f32 v73, v74, v75
	v_cvt_pk_bf16_f32 v74, v76, v77
	v_cvt_pk_bf16_f32 v75, v78, v79
	v_cvt_pk_bf16_f32 v64, v80, v81
	v_cvt_pk_bf16_f32 v65, v82, v83
	v_cvt_pk_bf16_f32 v66, v84, v85
	v_cvt_pk_bf16_f32 v67, v86, v87
	v_cvt_pk_bf16_f32 v68, v162, v163
	v_cvt_pk_bf16_f32 v69, v164, v165
	v_cvt_pk_bf16_f32 v70, v92, v93
	v_cvt_pk_bf16_f32 v71, v94, v95
	v_mfma_f32_32x32x16_bf16 v[96:111], v[166:169], v[170:173], v[96:111]
	v_lshl_add_u64 v[80:81], v[190:191], 0, s[6:7]
	global_load_dwordx4 v[162:165], v[80:81], off
	v_lshl_add_u64 v[80:81], v[192:193], 0, s[6:7]
	v_lshl_add_u64 v[76:77], v[188:189], 0, s[6:7]
	global_load_dwordx4 v[166:169], v[80:81], off
	v_lshl_add_u64 v[80:81], v[198:199], 0, s[6:7]
	global_load_dwordx4 v[76:79], v[76:77], off
	s_nop 0
	global_load_dwordx4 v[174:177], v[80:81], off
	global_load_dwordx4 v[170:173], v[186:187], off
	ds_read_b64_tr_b16 v[80:81], v201 offset:0
	ds_read_b64_tr_b16 v[82:83], v201 offset:0x800
	ds_read_b64_tr_b16 v[84:85], v201 offset:0x1000
	ds_read_b64_tr_b16 v[86:87], v201 offset:0x1800
	ds_read_b64_tr_b16 v[92:93], v201 offset:0x2000
	ds_read_b64_tr_b16 v[94:95], v201 offset:0x2800
	ds_read_b64_tr_b16 v[178:179], v201 offset:0x3000
	ds_read_b64_tr_b16 v[180:181], v201 offset:0x3800
	s_waitcnt lgkmcnt(0)
	s_nop 0
	v_mfma_f32_32x32x16_bf16 v[0:15], v[80:83], v[88:91], v[0:15]
	v_max_f32_e32 v80, v96, v97
	v_max3_f32 v81, v112, v113, v114
	v_max3_f32 v80, v80, v98, v99
	v_max3_f32 v81, v81, v115, v116
	v_max3_f32 v80, v80, v100, v101
	v_mfma_f32_32x32x16_bf16 v[0:15], v[84:87], v[72:75], v[0:15]
	v_max3_f32 v81, v81, v117, v118
	v_max3_f32 v80, v80, v102, v103
	v_max3_f32 v81, v81, v119, v120
	v_max3_f32 v80, v80, v104, v105
	v_max3_f32 v81, v81, v121, v122
	v_max3_f32 v80, v80, v106, v107
	v_max3_f32 v81, v81, v123, v124
	v_mfma_f32_32x32x16_bf16 v[0:15], v[92:95], v[64:67], v[0:15]
	v_max3_f32 v80, v80, v108, v109
	v_max3_f32 v81, v81, v125, v126
	v_max3_f32 v80, v80, v110, v111
	v_max3_f32 v194, v81, v127, v80
	ds_read_b64_tr_b16 v[80:81], v201 offset:0x200
	ds_read_b64_tr_b16 v[82:83], v201 offset:0xa00
	ds_read_b64_tr_b16 v[84:85], v201 offset:0x1200
	v_mfma_f32_32x32x16_bf16 v[0:15], v[178:181], v[68:71], v[0:15]
	ds_read_b64_tr_b16 v[86:87], v201 offset:0x1a00
	ds_read_b64_tr_b16 v[92:93], v201 offset:0x2200
	ds_read_b64_tr_b16 v[94:95], v201 offset:0x2a00
	ds_read_b64_tr_b16 v[178:179], v201 offset:0x3200
	ds_read_b64_tr_b16 v[180:181], v201 offset:0x3a00
	s_waitcnt lgkmcnt(0)
	v_mfma_f32_32x32x16_bf16 v[48:63], v[80:83], v[88:91], v[48:63]
	v_mov_b32_e32 v80, v194
	s_nop 1
	v_permlane32_swap_b32_e32 v194, v80
	v_max_f32_e32 v80, v194, v80
	v_sub_f32_e32 v81, v80, v227
	v_mfma_f32_32x32x16_bf16 v[48:63], v[84:87], v[72:75], v[48:63]
	v_cmp_ge_f32_e32 vcc, s34, v81
	v_mov_b32_e32 v202, 1.0
	s_cmp_eq_u64 vcc, exec
	s_cbranch_scc0 .Lmla_resc_0

.LBB0_863:
	s_waitcnt lgkmcnt(0)
	s_barrier
	ds_read_b128 v[64:67], v209 offset:32768
	ds_read_b128 v[68:71], v209 offset:40960
	ds_read_b128 v[162:165], v211 offset:32768
	ds_read_b128 v[166:169], v211 offset:40960
	v_exp_f32_e32 v112, v112
	v_exp_f32_e32 v113, v113
	s_waitcnt lgkmcnt(3)
	v_mfma_f32_32x32x16_bf16 v[96:111], v[64:67], v[158:161], 0
	v_exp_f32_e32 v114, v114
	v_exp_f32_e32 v115, v115
	v_exp_f32_e32 v116, v116
	v_exp_f32_e32 v117, v117
	v_exp_f32_e32 v118, v118
	v_exp_f32_e32 v119, v119
	s_waitcnt lgkmcnt(2)
	v_mfma_f32_32x32x16_bf16 v[64:79], v[68:71], v[158:161], 0
	s_waitcnt lgkmcnt(1)
	v_mfma_f32_32x32x16_bf16 v[96:111], v[162:165], v[154:157], v[96:111]
	s_waitcnt lgkmcnt(0)
	v_mfma_f32_32x32x16_bf16 v[64:79], v[166:169], v[154:157], v[64:79]
	ds_read_b128 v[162:165], v212 offset:32768
	ds_read_b128 v[166:169], v212 offset:40960
	s_waitcnt lgkmcnt(1)
	v_mfma_f32_32x32x16_bf16 v[96:111], v[162:165], v[150:153], v[96:111]
	s_waitcnt lgkmcnt(0)
	v_mfma_f32_32x32x16_bf16 v[64:79], v[166:169], v[150:153], v[64:79]
	ds_read_b128 v[162:165], v213 offset:32768
	ds_read_b128 v[166:169], v213 offset:40960
	s_waitcnt lgkmcnt(1)
	v_mfma_f32_32x32x16_bf16 v[96:111], v[162:165], v[146:149], v[96:111]
	s_waitcnt lgkmcnt(0)
	v_mfma_f32_32x32x16_bf16 v[64:79], v[166:169], v[146:149], v[64:79]
	ds_read_b128 v[162:165], v215 offset:32768
	ds_read_b128 v[166:169], v215 offset:40960
	s_waitcnt lgkmcnt(1)
	v_mfma_f32_32x32x16_bf16 v[96:111], v[162:165], v[142:145], v[96:111]
	s_waitcnt lgkmcnt(0)
	v_mfma_f32_32x32x16_bf16 v[64:79], v[166:169], v[142:145], v[64:79]
	ds_read_b128 v[162:165], v217 offset:32768
	ds_read_b128 v[166:169], v217 offset:40960
	s_waitcnt lgkmcnt(1)
	v_mfma_f32_32x32x16_bf16 v[96:111], v[162:165], v[138:141], v[96:111]
	s_waitcnt lgkmcnt(0)
	v_mfma_f32_32x32x16_bf16 v[64:79], v[166:169], v[138:141], v[64:79]
	ds_read_b128 v[162:165], v214 offset:32768
	ds_read_b128 v[166:169], v214 offset:40960
	s_waitcnt lgkmcnt(1)
	v_mfma_f32_32x32x16_bf16 v[96:111], v[162:165], v[134:137], v[96:111]
	s_waitcnt lgkmcnt(0)
	v_mfma_f32_32x32x16_bf16 v[64:79], v[166:169], v[134:137], v[64:79]
	ds_read_b128 v[162:165], v216 offset:32768
	ds_read_b128 v[166:169], v216 offset:40960
	s_waitcnt lgkmcnt(1)
	v_mfma_f32_32x32x16_bf16 v[96:111], v[162:165], v[130:133], v[96:111]
	s_waitcnt lgkmcnt(0)
	v_mfma_f32_32x32x16_bf16 v[64:79], v[166:169], v[130:133], v[64:79]
	ds_read_b128 v[162:165], v219
	ds_read_b128 v[166:169], v219 offset:4096
	ds_read_b128 v[170:173], v204
	s_waitcnt lgkmcnt(0)
	v_mfma_f32_32x32x16_bf16 v[96:111], v[162:165], v[170:173], v[96:111]
	v_mfma_f32_32x32x16_bf16 v[64:79], v[166:169], v[170:173], v[64:79]
	ds_read_b128 v[162:165], v221
	ds_read_b128 v[166:169], v221 offset:4096
	ds_read_b128 v[170:173], v204 offset:1024
	s_waitcnt lgkmcnt(0)
	v_mfma_f32_32x32x16_bf16 v[96:111], v[162:165], v[170:173], v[96:111]
	v_mfma_f32_32x32x16_bf16 v[64:79], v[166:169], v[170:173], v[64:79]
	ds_read_b128 v[162:165], v223
	ds_read_b128 v[166:169], v223 offset:4096
	ds_read_b128 v[170:173], v204 offset:2048
	s_waitcnt lgkmcnt(0)
	v_mfma_f32_32x32x16_bf16 v[96:111], v[162:165], v[170:173], v[96:111]
	v_mfma_f32_32x32x16_bf16 v[64:79], v[166:169], v[170:173], v[64:79]
	ds_read_b128 v[162:165], v225
	ds_read_b128 v[166:169], v225 offset:4096
	ds_read_b128 v[170:173], v204 offset:3072
	s_waitcnt lgkmcnt(0)
	v_mfma_f32_32x32x16_bf16 v[96:111], v[162:165], v[170:173], v[96:111]
	v_exp_f32_e32 v162, v120
	v_exp_f32_e32 v163, v121
	v_exp_f32_e32 v164, v122
	v_exp_f32_e32 v165, v123
	v_add_f32_e32 v120, v80, v81
	v_add_f32_e32 v121, v88, v89
	v_add_f32_e32 v122, v112, v113
	v_mfma_f32_32x32x16_bf16 v[64:79], v[166:169], v[170:173], v[64:79]
	v_exp_f32_e32 v166, v124
	v_exp_f32_e32 v167, v125
	v_add_f32_e32 v123, v162, v163
	v_exp_f32_e32 v168, v126
	v_add_f32_e32 v120, v82, v120
	v_add_f32_e32 v121, v90, v121
	v_add_f32_e32 v122, v114, v122
	v_add_f32_e32 v123, v164, v123
	v_exp_f32_e32 v169, v127
	v_add_f32_e32 v120, v83, v120
	v_add_f32_e32 v121, v91, v121
	v_add_f32_e32 v122, v115, v122
	v_add_f32_e32 v123, v165, v123
	v_add_f32_e32 v120, v84, v120
	v_add_f32_e32 v121, v92, v121
	v_add_f32_e32 v122, v116, v122
	v_add_f32_e32 v123, v166, v123
	v_add_f32_e32 v120, v85, v120
	v_add_f32_e32 v121, v93, v121
	v_add_f32_e32 v122, v117, v122
	v_add_f32_e32 v123, v167, v123
	v_add_f32_e32 v120, v86, v120
	v_add_f32_e32 v121, v94, v121
	v_add_f32_e32 v122, v118, v122
	v_add_f32_e32 v123, v168, v123
	v_add_f32_e32 v120, v87, v120
	v_add_f32_e32 v121, v95, v121
	v_add_f32_e32 v122, v119, v122
	v_add_f32_e32 v123, v169, v123
	v_add_f32_e32 v120, v121, v120
	v_add_f32_e32 v121, v123, v122
	v_add_f32_e32 v239, v120, v121
	v_cvt_pk_bf16_f32 v124, v80, v81
	v_cvt_pk_bf16_f32 v125, v82, v83
	v_cvt_pk_bf16_f32 v126, v84, v85
	v_cvt_pk_bf16_f32 v127, v86, v87
	v_cvt_pk_bf16_f32 v120, v88, v89
	v_cvt_pk_bf16_f32 v121, v90, v91
	v_cvt_pk_bf16_f32 v122, v92, v93
	v_cvt_pk_bf16_f32 v123, v94, v95
	v_cvt_pk_bf16_f32 v112, v112, v113
	v_cvt_pk_bf16_f32 v113, v114, v115
	v_cvt_pk_bf16_f32 v114, v116, v117
	v_cvt_pk_bf16_f32 v115, v118, v119
	v_cvt_pk_bf16_f32 v116, v162, v163
	v_cvt_pk_bf16_f32 v117, v164, v165
	v_cvt_pk_bf16_f32 v118, v166, v167
	v_cvt_pk_bf16_f32 v119, v168, v169
	s_add_i32 s2, s20, 1
	s_min_i32 s2, s2, s23
	s_lshl_b32 s72, s2, 6
	s_mul_i32 s2, s72, s62
	s_mov_b32 s3, s73
	s_lshl_b64 s[2:3], s[2:3], 1
	s_add_u32 s24, s18, s2
	s_addc_u32 s25, s19, s3
	s_add_u32 s2, s16, s2
	s_addc_u32 s3, s17, s3
	global_load_dwordx4 v[162:165], v128, s[24:25]
	global_load_dwordx4 v[166:169], v182, s[24:25]
	global_load_dwordx4 v[170:173], v128, s[2:3]
	global_load_dwordx4 v[174:177], v182, s[2:3]
	s_lshl_b64 s[2:3], s[72:73], 7
	v_lshl_add_u64 v[80:81], v[184:185], 0, s[2:3]
	global_load_dwordx4 v[178:181], v[80:81], off
	ds_read_b64_tr_b16 v[80:81], v203 offset:0
	ds_read_b64_tr_b16 v[82:83], v203 offset:0x800
	ds_read_b64_tr_b16 v[84:85], v203 offset:0x1000
	ds_read_b64_tr_b16 v[86:87], v203 offset:0x1800
	ds_read_b64_tr_b16 v[88:89], v203 offset:0x2000
	ds_read_b64_tr_b16 v[90:91], v203 offset:0x2800
	ds_read_b64_tr_b16 v[92:93], v203 offset:0x3000
	ds_read_b64_tr_b16 v[94:95], v203 offset:0x3800
	s_waitcnt lgkmcnt(0)
	s_nop 0
	v_mfma_f32_32x32x16_bf16 v[0:15], v[80:83], v[124:127], v[0:15]
	v_max_f32_e32 v80, v64, v65
	v_max3_f32 v81, v96, v97, v98
	v_max3_f32 v80, v80, v66, v67
	v_max3_f32 v81, v81, v99, v100
	v_max3_f32 v80, v80, v68, v69
	v_mfma_f32_32x32x16_bf16 v[0:15], v[84:87], v[120:123], v[0:15]
	v_max3_f32 v81, v81, v101, v102
	v_max3_f32 v80, v80, v70, v71
	v_max3_f32 v81, v81, v103, v104
	v_max3_f32 v80, v80, v72, v73
	v_max3_f32 v81, v81, v105, v106
	v_max3_f32 v80, v80, v74, v75
	v_max3_f32 v81, v81, v107, v108
	v_mfma_f32_32x32x16_bf16 v[0:15], v[88:91], v[112:115], v[0:15]
	v_max3_f32 v80, v80, v76, v77
	v_max3_f32 v81, v81, v109, v110
	v_max3_f32 v80, v80, v78, v79
	v_max3_f32 v194, v81, v111, v80
	ds_read_b64_tr_b16 v[80:81], v203 offset:0x200
	ds_read_b64_tr_b16 v[82:83], v203 offset:0xa00
	ds_read_b64_tr_b16 v[84:85], v203 offset:0x1200
	v_mfma_f32_32x32x16_bf16 v[0:15], v[92:95], v[116:119], v[0:15]
	ds_read_b64_tr_b16 v[86:87], v203 offset:0x1a00
	ds_read_b64_tr_b16 v[88:89], v203 offset:0x2200
	ds_read_b64_tr_b16 v[90:91], v203 offset:0x2a00
	ds_read_b64_tr_b16 v[92:93], v203 offset:0x3200
	ds_read_b64_tr_b16 v[94:95], v203 offset:0x3a00
	s_waitcnt lgkmcnt(0)
	v_mfma_f32_32x32x16_bf16 v[48:63], v[80:83], v[124:127], v[48:63]
	v_mov_b32_e32 v80, v194
	s_nop 1
	v_permlane32_swap_b32_e32 v194, v80
	v_max_f32_e32 v80, v194, v80
	v_sub_f32_e32 v81, v80, v227
	v_mfma_f32_32x32x16_bf16 v[48:63], v[84:87], v[120:123], v[48:63]
	v_cmp_ge_f32_e32 vcc, s34, v81
	v_mov_b32_e32 v200, 1.0
	s_cmp_eq_u64 vcc, exec
	s_cbranch_scc0 .Lmla_resc_1

.LBB0_865:
	v_fma_f32 v96, v210, v226, v237
	s_add_i32 s20, s20, 2
	v_fma_f32 v210, v96, v202, v239
	v_lshl_add_u64 v[186:187], v[186:187], 0, s[56:57]
	v_lshl_add_u64 v[188:189], v[188:189], 0, s[10:11]
	v_lshl_add_u64 v[190:191], v[190:191], 0, s[10:11]
	v_lshl_add_u64 v[192:193], v[192:193], 0, s[10:11]
	s_cmp_ge_u32 s20, s22
	v_lshl_add_u64 v[198:199], v[198:199], 0, s[10:11]
	s_waitcnt lgkmcnt(0)
	s_barrier
	s_cbranch_scc1 .LBB0_867
	v_mov_b32_e32 v226, v200
	s_branch .LBB0_861
